# P8 SwiGLU epilogue: the two constant multiplies before v_exp folded into one (64 places)
# baseline (speedup 1.0000x reference)
.LBB0_1126:
	s_lshl_b32 s4, s92, 10
	s_and_b32 s4, s4, 0x400
	s_nop 15
	s_nop 15
	v_add_u32_e32 v2, s4, v203
	ds_read_b128 v[14:17], v2
	ds_read_b128 v[10:13], v2 offset:16
	ds_read_b128 v[6:9], v2 offset:512
	ds_read_b128 v[2:5], v2 offset:528
	v_lshl_or_b32 v22, s8, 7, v238
	s_waitcnt lgkmcnt(0)
	v_pk_fma_f32 v[26:27], v[194:195], s[38:39], v[14:15] op_sel_hi:[1,0,1]
	v_pk_fma_f32 v[18:19], v[196:197], s[38:39], v[16:17] op_sel_hi:[1,0,1]
	v_min_f32_e32 v26, 0x40e00000, v26
	v_mul_f32_e32 v36, 0xc01d265f, v26
	v_exp_f32_e32 v36, v36
	v_pk_fma_f32 v[32:33], v[186:187], s[38:39], v[6:7] op_sel_hi:[1,0,1]
	v_min_f32_e32 v27, 0x40e00000, v27
	v_med3_f32 v32, v32, s93, v242
	v_add_f32_e32 v36, 1.0, v36
	v_rcp_f32_e32 v36, v36
	v_add_f32_e32 v32, 1.0, v32
	v_min_f32_e32 v18, 0x40e00000, v18
	v_pk_fma_f32 v[30:31], v[188:189], s[38:39], v[8:9] op_sel_hi:[1,0,1]
	v_mul_f32_e32 v26, v26, v36
	v_mul_f32_e32 v26, v32, v26
	v_med3_f32 v32, v33, s93, v242
	v_mul_f32_e32 v33, 0xc01d265f, v27
	v_exp_f32_e32 v33, v33
	v_add_f32_e32 v32, 1.0, v32
	v_med3_f32 v30, v30, s93, v242
	v_add_f32_e32 v30, 1.0, v30
	v_add_f32_e32 v33, 1.0, v33
	v_rcp_f32_e32 v33, v33
	v_pk_fma_f32 v[28:29], v[190:191], s[38:39], v[10:11] op_sel_hi:[1,0,1]
	v_pk_fma_f32 v[34:35], v[182:183], s[38:39], v[2:3] op_sel_hi:[1,0,1]
	v_pk_fma_f32 v[20:21], v[192:193], s[38:39], v[12:13] op_sel_hi:[1,0,1]
	v_mul_f32_e32 v27, v27, v33
	v_mul_f32_e32 v27, v32, v27
	v_mul_f32_e32 v32, 0xc01d265f, v18
	v_exp_f32_e32 v32, v32
	v_pk_fma_f32 v[24:25], v[184:185], s[38:39], v[4:5] op_sel_hi:[1,0,1]
	v_pk_fma_f32 v[36:37], v[166:167], s[38:39], v[2:3] op_sel_hi:[1,0,1]
	v_ashrrev_i32_e32 v23, 31, v22
	v_add_f32_e32 v32, 1.0, v32
	v_rcp_f32_e32 v32, v32
	s_and_b64 vcc, exec, s[2:3]
	v_mul_f32_e32 v18, v18, v32
	v_mul_f32_e32 v30, v30, v18
	v_min_f32_e32 v18, 0x40e00000, v19
	v_med3_f32 v19, v31, s93, v242
	v_mul_f32_e32 v31, 0xc01d265f, v18
	v_exp_f32_e32 v31, v31
	v_add_f32_e32 v19, 1.0, v19
	v_pk_fma_f32 v[32:33], v[172:173], s[38:39], v[8:9] op_sel_hi:[1,0,1]
	v_add_f32_e32 v31, 1.0, v31
	v_rcp_f32_e32 v31, v31
	v_med3_f32 v32, v32, s93, v242
	v_add_f32_e32 v32, 1.0, v32
	v_mul_f32_e32 v18, v18, v31
	v_mul_f32_e32 v19, v19, v18
	v_mov_b32_e32 v18, v67
	v_cvt_pk_fp8_f32 v18, v26, v27
	v_med3_f32 v26, v34, s93, v242
	v_add_f32_e32 v26, 1.0, v26
	v_cvt_pk_fp8_f32 v18, v30, v19 op_sel:[0,0,1]
	v_min_f32_e32 v19, 0x40e00000, v28
	v_mul_f32_e32 v27, 0xc01d265f, v19
	v_exp_f32_e32 v27, v27
	v_pk_fma_f32 v[30:31], v[174:175], s[38:39], v[10:11] op_sel_hi:[1,0,1]
	v_add_f32_e32 v27, 1.0, v27
	v_rcp_f32_e32 v27, v27
	s_nop 0
	v_mul_f32_e32 v19, v19, v27
	v_mul_f32_e32 v26, v26, v19
	v_min_f32_e32 v19, 0x40e00000, v29
	v_mul_f32_e32 v28, 0xc01d265f, v19
	v_exp_f32_e32 v28, v28
	v_med3_f32 v27, v35, s93, v242
	v_add_f32_e32 v27, 1.0, v27
	v_pk_fma_f32 v[34:35], v[170:171], s[38:39], v[6:7] op_sel_hi:[1,0,1]
	v_add_f32_e32 v28, 1.0, v28
	v_rcp_f32_e32 v28, v28
	v_med3_f32 v34, v34, s93, v242
	v_add_f32_e32 v34, 1.0, v34
	v_mul_f32_e32 v19, v19, v28
	v_mul_f32_e32 v27, v27, v19
	v_min_f32_e32 v19, 0x40e00000, v20
	v_med3_f32 v20, v24, s93, v242
	v_mul_f32_e32 v24, 0xc01d265f, v19
	v_exp_f32_e32 v24, v24
	v_pk_fma_f32 v[28:29], v[178:179], s[38:39], v[14:15] op_sel_hi:[1,0,1]
	v_add_f32_e32 v20, 1.0, v20
	v_min_f32_e32 v28, 0x40e00000, v28
	v_add_f32_e32 v24, 1.0, v24
	v_rcp_f32_e32 v24, v24
	v_mul_f32_e32 v38, 0xc01d265f, v28
	v_exp_f32_e32 v38, v38
	v_mul_f32_e32 v19, v19, v24
	v_mul_f32_e32 v20, v20, v19
	v_min_f32_e32 v19, 0x40e00000, v21
	v_mul_f32_e32 v24, 0xc01d265f, v19
	v_add_f32_e32 v38, 1.0, v38
	v_exp_f32_e32 v24, v24
	v_rcp_f32_e32 v38, v38
	v_min_f32_e32 v29, 0x40e00000, v29
	v_med3_f32 v21, v25, s93, v242
	v_add_f32_e32 v24, 1.0, v24
	v_mul_f32_e32 v28, v28, v38
	v_rcp_f32_e32 v24, v24
	v_mul_f32_e32 v28, v34, v28
	v_med3_f32 v34, v35, s93, v242
	v_mul_f32_e32 v35, 0xc01d265f, v29
	v_exp_f32_e32 v35, v35
	v_mul_f32_e32 v19, v19, v24
	v_add_f32_e32 v21, 1.0, v21
	v_mul_f32_e32 v21, v21, v19
	v_mov_b32_e32 v19, v67
	v_cvt_pk_fp8_f32 v19, v26, v27
	v_add_f32_e32 v35, 1.0, v35
	v_rcp_f32_e32 v35, v35
	v_add_f32_e32 v34, 1.0, v34
	v_cvt_pk_fp8_f32 v19, v20, v21 op_sel:[0,0,1]
	v_pk_fma_f32 v[20:21], v[180:181], s[38:39], v[16:17] op_sel_hi:[1,0,1]
	v_mul_f32_e32 v29, v29, v35
	v_min_f32_e32 v20, 0x40e00000, v20
	v_mul_f32_e32 v29, v34, v29
	v_mul_f32_e32 v34, 0xc01d265f, v20
	v_exp_f32_e32 v34, v34
	v_pk_fma_f32 v[24:25], v[176:177], s[38:39], v[12:13] op_sel_hi:[1,0,1]
	v_pk_fma_f32 v[26:27], v[168:169], s[38:39], v[4:5] op_sel_hi:[1,0,1]
	v_add_f32_e32 v34, 1.0, v34
	v_rcp_f32_e32 v34, v34
	s_nop 0
	v_mul_f32_e32 v20, v20, v34
	v_mul_f32_e32 v32, v32, v20
	v_min_f32_e32 v20, 0x40e00000, v21
	v_med3_f32 v21, v33, s93, v242
	v_mul_f32_e32 v33, 0xc01d265f, v20
	v_exp_f32_e32 v33, v33
	v_add_f32_e32 v21, 1.0, v21
	v_pk_fma_f32 v[34:35], v[150:151], s[38:39], v[2:3] op_sel_hi:[1,0,1]
	v_add_f32_e32 v33, 1.0, v33
	v_rcp_f32_e32 v33, v33
	s_nop 0
	v_mul_f32_e32 v20, v20, v33
	v_mul_f32_e32 v21, v21, v20
	v_mov_b32_e32 v20, v67
	v_cvt_pk_fp8_f32 v20, v28, v29
	v_med3_f32 v28, v36, s93, v242
	v_add_f32_e32 v28, 1.0, v28
	v_cvt_pk_fp8_f32 v20, v32, v21 op_sel:[0,0,1]
	v_min_f32_e32 v21, 0x40e00000, v30
	v_mul_f32_e32 v29, 0xc01d265f, v21
	v_exp_f32_e32 v29, v29
	v_pk_fma_f32 v[32:33], v[154:155], s[38:39], v[6:7] op_sel_hi:[1,0,1]
	v_permlane32_swap_b32_e32 v18, v20
	v_add_f32_e32 v29, 1.0, v29
	v_rcp_f32_e32 v29, v29
	v_med3_f32 v32, v32, s93, v242
	v_add_f32_e32 v32, 1.0, v32
	v_mul_f32_e32 v21, v21, v29
	v_mul_f32_e32 v28, v28, v21
	v_min_f32_e32 v21, 0x40e00000, v31
	v_mul_f32_e32 v30, 0xc01d265f, v21
	v_exp_f32_e32 v30, v30
	v_med3_f32 v29, v37, s93, v242
	v_add_f32_e32 v29, 1.0, v29
	v_add_f32_e32 v30, 1.0, v30
	v_rcp_f32_e32 v30, v30
	s_nop 0
	v_mul_f32_e32 v21, v21, v30
	v_mul_f32_e32 v29, v29, v21
	v_min_f32_e32 v21, 0x40e00000, v24
	v_med3_f32 v24, v26, s93, v242
	v_mul_f32_e32 v26, 0xc01d265f, v21
	v_exp_f32_e32 v26, v26
	v_add_f32_e32 v24, 1.0, v24
	v_pk_fma_f32 v[30:31], v[156:157], s[38:39], v[8:9] op_sel_hi:[1,0,1]
	v_add_f32_e32 v26, 1.0, v26
	v_rcp_f32_e32 v26, v26
	v_med3_f32 v30, v30, s93, v242
	v_add_f32_e32 v30, 1.0, v30
	v_mul_f32_e32 v21, v21, v26
	v_mul_f32_e32 v24, v24, v21
	v_min_f32_e32 v21, 0x40e00000, v25
	v_mul_f32_e32 v26, 0xc01d265f, v21
	v_exp_f32_e32 v26, v26
	v_med3_f32 v25, v27, s93, v242
	v_add_f32_e32 v25, 1.0, v25
	v_add_f32_e32 v26, 1.0, v26
	v_rcp_f32_e32 v26, v26
	s_nop 0
	v_mul_f32_e32 v21, v21, v26
	v_pk_fma_f32 v[26:27], v[162:163], s[38:39], v[14:15] op_sel_hi:[1,0,1]
	v_mul_f32_e32 v25, v25, v21
	v_min_f32_e32 v26, 0x40e00000, v26
	v_mul_f32_e32 v36, 0xc01d265f, v26
	v_exp_f32_e32 v36, v36
	v_min_f32_e32 v27, 0x40e00000, v27
	v_mov_b32_e32 v21, v67
	v_cvt_pk_fp8_f32 v21, v28, v29
	v_add_f32_e32 v36, 1.0, v36
	v_rcp_f32_e32 v36, v36
	v_pk_fma_f32 v[28:29], v[158:159], s[38:39], v[10:11] op_sel_hi:[1,0,1]
	v_cvt_pk_fp8_f32 v21, v24, v25 op_sel:[0,0,1]
	v_add_u32_e32 v24, s83, v218
	v_mul_f32_e32 v26, v26, v36
	v_mul_f32_e32 v26, v32, v26
	v_med3_f32 v32, v33, s93, v242
	v_mul_f32_e32 v33, 0xc01d265f, v27
	v_exp_f32_e32 v33, v33
	v_ashrrev_i32_e32 v25, 31, v24
	v_lshlrev_b64 v[24:25], 11, v[24:25]
	v_lshl_add_u64 v[24:25], s[12:13], 0, v[24:25]
	v_add_f32_e32 v33, 1.0, v33
	v_rcp_f32_e32 v33, v33
	v_permlane32_swap_b32_e32 v19, v21
	v_lshl_add_u64 v[24:25], v[24:25], 0, v[22:23]
	global_store_dwordx4 v[24:25], v[18:21], off
	v_mul_f32_e32 v27, v27, v33
	v_add_f32_e32 v32, 1.0, v32
	v_pk_fma_f32 v[18:19], v[164:165], s[38:39], v[16:17] op_sel_hi:[1,0,1]
	v_mul_f32_e32 v27, v32, v27
	v_min_f32_e32 v18, 0x40e00000, v18
	v_mul_f32_e32 v32, 0xc01d265f, v18
	v_exp_f32_e32 v32, v32
	v_pk_fma_f32 v[20:21], v[160:161], s[38:39], v[12:13] op_sel_hi:[1,0,1]
	v_pk_fma_f32 v[24:25], v[152:153], s[38:39], v[4:5] op_sel_hi:[1,0,1]
	v_pk_fma_f32 v[36:37], v[134:135], s[38:39], v[2:3] op_sel_hi:[1,0,1]
	v_add_f32_e32 v32, 1.0, v32
	v_rcp_f32_e32 v32, v32
	s_nop 0
	v_mul_f32_e32 v18, v18, v32
	v_mul_f32_e32 v30, v30, v18
	v_min_f32_e32 v18, 0x40e00000, v19
	v_med3_f32 v19, v31, s93, v242
	v_mul_f32_e32 v31, 0xc01d265f, v18
	v_exp_f32_e32 v31, v31
	v_add_f32_e32 v19, 1.0, v19
	v_pk_fma_f32 v[32:33], v[140:141], s[38:39], v[8:9] op_sel_hi:[1,0,1]
	v_add_f32_e32 v31, 1.0, v31
	v_rcp_f32_e32 v31, v31
	v_med3_f32 v32, v32, s93, v242
	v_add_f32_e32 v32, 1.0, v32
	v_mul_f32_e32 v18, v18, v31
	v_mul_f32_e32 v19, v19, v18
	v_mov_b32_e32 v18, v67
	v_cvt_pk_fp8_f32 v18, v26, v27
	v_med3_f32 v26, v34, s93, v242
	v_add_f32_e32 v26, 1.0, v26
	v_cvt_pk_fp8_f32 v18, v30, v19 op_sel:[0,0,1]
	v_min_f32_e32 v19, 0x40e00000, v28
	v_mul_f32_e32 v27, 0xc01d265f, v19
	v_exp_f32_e32 v27, v27
	v_pk_fma_f32 v[30:31], v[142:143], s[38:39], v[10:11] op_sel_hi:[1,0,1]
	v_add_f32_e32 v27, 1.0, v27
	v_rcp_f32_e32 v27, v27
	s_nop 0
	v_mul_f32_e32 v19, v19, v27
	v_mul_f32_e32 v26, v26, v19
	v_min_f32_e32 v19, 0x40e00000, v29
	v_mul_f32_e32 v28, 0xc01d265f, v19
	v_exp_f32_e32 v28, v28
	v_med3_f32 v27, v35, s93, v242
	v_add_f32_e32 v27, 1.0, v27
	v_pk_fma_f32 v[34:35], v[138:139], s[38:39], v[6:7] op_sel_hi:[1,0,1]
	v_add_f32_e32 v28, 1.0, v28
	v_rcp_f32_e32 v28, v28
	v_med3_f32 v34, v34, s93, v242
	v_add_f32_e32 v34, 1.0, v34
	v_mul_f32_e32 v19, v19, v28
	v_mul_f32_e32 v27, v27, v19
	v_min_f32_e32 v19, 0x40e00000, v20
	v_med3_f32 v20, v24, s93, v242
	v_mul_f32_e32 v24, 0xc01d265f, v19
	v_exp_f32_e32 v24, v24
	v_pk_fma_f32 v[28:29], v[146:147], s[38:39], v[14:15] op_sel_hi:[1,0,1]
	v_add_f32_e32 v20, 1.0, v20
	v_min_f32_e32 v28, 0x40e00000, v28
	v_add_f32_e32 v24, 1.0, v24
	v_rcp_f32_e32 v24, v24
	v_mul_f32_e32 v38, 0xc01d265f, v28
	v_exp_f32_e32 v38, v38
	v_mul_f32_e32 v19, v19, v24
	v_mul_f32_e32 v20, v20, v19
	v_min_f32_e32 v19, 0x40e00000, v21
	v_mul_f32_e32 v24, 0xc01d265f, v19
	v_add_f32_e32 v38, 1.0, v38
	v_exp_f32_e32 v24, v24
	v_rcp_f32_e32 v38, v38
	v_min_f32_e32 v29, 0x40e00000, v29
	v_med3_f32 v21, v25, s93, v242
	v_add_f32_e32 v24, 1.0, v24
	v_mul_f32_e32 v28, v28, v38
	v_rcp_f32_e32 v24, v24
	v_mul_f32_e32 v28, v34, v28
	v_med3_f32 v34, v35, s93, v242
	v_mul_f32_e32 v35, 0xc01d265f, v29
	v_exp_f32_e32 v35, v35
	v_mul_f32_e32 v19, v19, v24
	v_add_f32_e32 v21, 1.0, v21
	v_mul_f32_e32 v21, v21, v19
	v_mov_b32_e32 v19, v67
	v_cvt_pk_fp8_f32 v19, v26, v27
	v_add_f32_e32 v35, 1.0, v35
	v_rcp_f32_e32 v35, v35
	v_add_f32_e32 v34, 1.0, v34
	v_cvt_pk_fp8_f32 v19, v20, v21 op_sel:[0,0,1]
	v_pk_fma_f32 v[20:21], v[148:149], s[38:39], v[16:17] op_sel_hi:[1,0,1]
	v_mul_f32_e32 v29, v29, v35
	v_min_f32_e32 v20, 0x40e00000, v20
	v_mul_f32_e32 v29, v34, v29
	v_mul_f32_e32 v34, 0xc01d265f, v20
	v_exp_f32_e32 v34, v34
	v_pk_fma_f32 v[24:25], v[144:145], s[38:39], v[12:13] op_sel_hi:[1,0,1]
	v_pk_fma_f32 v[26:27], v[136:137], s[38:39], v[4:5] op_sel_hi:[1,0,1]
	v_add_f32_e32 v34, 1.0, v34
	v_rcp_f32_e32 v34, v34
	s_nop 0
	v_mul_f32_e32 v20, v20, v34
	v_mul_f32_e32 v32, v32, v20
	v_min_f32_e32 v20, 0x40e00000, v21
	v_med3_f32 v21, v33, s93, v242
	v_mul_f32_e32 v33, 0xc01d265f, v20
	v_exp_f32_e32 v33, v33
	v_add_f32_e32 v21, 1.0, v21
	v_add_f32_e32 v33, 1.0, v33
	v_rcp_f32_e32 v33, v33
	s_nop 0
	v_mul_f32_e32 v20, v20, v33
	v_mul_f32_e32 v21, v21, v20
	v_mov_b32_e32 v20, v67
	v_cvt_pk_fp8_f32 v20, v28, v29
	v_med3_f32 v28, v36, s93, v242
	v_add_f32_e32 v28, 1.0, v28
	v_cvt_pk_fp8_f32 v20, v32, v21 op_sel:[0,0,1]
	v_min_f32_e32 v21, 0x40e00000, v30
	v_mul_f32_e32 v29, 0xc01d265f, v21
	v_exp_f32_e32 v29, v29
	v_permlane32_swap_b32_e32 v18, v20
	v_add_f32_e32 v29, 1.0, v29
	v_rcp_f32_e32 v29, v29
	s_nop 0
	v_mul_f32_e32 v21, v21, v29
	v_mul_f32_e32 v28, v28, v21
	v_min_f32_e32 v21, 0x40e00000, v31
	v_mul_f32_e32 v30, 0xc01d265f, v21
	v_exp_f32_e32 v30, v30
	v_med3_f32 v29, v37, s93, v242
	v_add_f32_e32 v29, 1.0, v29
	v_add_f32_e32 v30, 1.0, v30
	v_rcp_f32_e32 v30, v30
	s_nop 0
	v_mul_f32_e32 v21, v21, v30
	v_mul_f32_e32 v29, v29, v21
	v_min_f32_e32 v21, 0x40e00000, v24
	v_med3_f32 v24, v26, s93, v242
	v_mul_f32_e32 v26, 0xc01d265f, v21
	v_exp_f32_e32 v26, v26
	v_add_f32_e32 v24, 1.0, v24
	v_add_f32_e32 v26, 1.0, v26
	v_rcp_f32_e32 v26, v26
	s_nop 0
	v_mul_f32_e32 v21, v21, v26
	v_mul_f32_e32 v24, v24, v21
	v_min_f32_e32 v21, 0x40e00000, v25
	v_mul_f32_e32 v26, 0xc01d265f, v21
	v_exp_f32_e32 v26, v26
	v_med3_f32 v25, v27, s93, v242
	v_add_f32_e32 v25, 1.0, v25
	v_add_f32_e32 v26, 1.0, v26
	v_rcp_f32_e32 v26, v26
	s_nop 0
	v_mul_f32_e32 v21, v21, v26
	v_mul_f32_e32 v25, v25, v21
	v_mov_b32_e32 v21, v67
	v_cvt_pk_fp8_f32 v21, v28, v29
	v_cvt_pk_fp8_f32 v21, v24, v25 op_sel:[0,0,1]
	v_add_u32_e32 v24, s83, v219
	v_ashrrev_i32_e32 v25, 31, v24
	v_lshlrev_b64 v[24:25], 11, v[24:25]
	v_lshl_add_u64 v[24:25], s[12:13], 0, v[24:25]
	v_permlane32_swap_b32_e32 v19, v21
	v_lshl_add_u64 v[24:25], v[24:25], 0, v[22:23]
	global_store_dwordx4 v[24:25], v[18:21], off
	s_cbranch_vccz .LBB0_1128
	s_cmp_lg_u32 s92, s68
	s_cbranch_scc0 .LBB0_1129
	s_branch .LBB0_1140
.LBB0_1128:
	v_pk_fma_f32 v[26:27], v[130:131], s[38:39], v[14:15] op_sel_hi:[1,0,1]
	v_pk_fma_f32 v[32:33], v[122:123], s[38:39], v[6:7] op_sel_hi:[1,0,1]
	v_min_f32_e32 v26, 0x40e00000, v26
	v_mul_f32_e32 v36, 0xc01d265f, v26
	v_exp_f32_e32 v36, v36
	v_med3_f32 v32, v32, s93, v242
	v_add_f32_e32 v32, 1.0, v32
	v_min_f32_e32 v27, 0x40e00000, v27
	v_add_f32_e32 v36, 1.0, v36
	v_rcp_f32_e32 v36, v36
	v_pk_fma_f32 v[18:19], v[132:133], s[38:39], v[16:17] op_sel_hi:[1,0,1]
	v_pk_fma_f32 v[30:31], v[124:125], s[38:39], v[8:9] op_sel_hi:[1,0,1]
	v_min_f32_e32 v18, 0x40e00000, v18
	v_mul_f32_e32 v26, v26, v36
	v_mul_f32_e32 v26, v32, v26
	v_med3_f32 v32, v33, s93, v242
	v_mul_f32_e32 v33, 0xc01d265f, v27
	v_exp_f32_e32 v33, v33
	v_add_f32_e32 v32, 1.0, v32
	v_med3_f32 v30, v30, s93, v242
	v_add_f32_e32 v30, 1.0, v30
	v_add_f32_e32 v33, 1.0, v33
	v_rcp_f32_e32 v33, v33
	v_pk_fma_f32 v[28:29], v[126:127], s[38:39], v[10:11] op_sel_hi:[1,0,1]
	v_pk_fma_f32 v[34:35], v[118:119], s[38:39], v[2:3] op_sel_hi:[1,0,1]
	v_pk_fma_f32 v[20:21], v[128:129], s[38:39], v[12:13] op_sel_hi:[1,0,1]
	v_mul_f32_e32 v27, v27, v33
	v_mul_f32_e32 v27, v32, v27
	v_mul_f32_e32 v32, 0xc01d265f, v18
	v_exp_f32_e32 v32, v32
	v_pk_fma_f32 v[24:25], v[120:121], s[38:39], v[4:5] op_sel_hi:[1,0,1]
	v_pk_fma_f32 v[36:37], v[102:103], s[38:39], v[2:3] op_sel_hi:[1,0,1]
	v_add_f32_e32 v32, 1.0, v32
	v_rcp_f32_e32 v32, v32
	s_nop 0
	v_mul_f32_e32 v18, v18, v32
	v_mul_f32_e32 v30, v30, v18
	v_min_f32_e32 v18, 0x40e00000, v19
	v_med3_f32 v19, v31, s93, v242
	v_mul_f32_e32 v31, 0xc01d265f, v18
	v_exp_f32_e32 v31, v31
	v_add_f32_e32 v19, 1.0, v19
	v_pk_fma_f32 v[32:33], v[108:109], s[38:39], v[8:9] op_sel_hi:[1,0,1]
	v_add_f32_e32 v31, 1.0, v31
	v_rcp_f32_e32 v31, v31
	v_med3_f32 v32, v32, s93, v242
	v_add_f32_e32 v32, 1.0, v32
	v_mul_f32_e32 v18, v18, v31
	v_mul_f32_e32 v19, v19, v18
	v_mov_b32_e32 v18, v67
	v_cvt_pk_fp8_f32 v18, v26, v27
	v_med3_f32 v26, v34, s93, v242
	v_add_f32_e32 v26, 1.0, v26
	v_cvt_pk_fp8_f32 v18, v30, v19 op_sel:[0,0,1]
	v_min_f32_e32 v19, 0x40e00000, v28
	v_mul_f32_e32 v27, 0xc01d265f, v19
	v_exp_f32_e32 v27, v27
	v_pk_fma_f32 v[30:31], v[110:111], s[38:39], v[10:11] op_sel_hi:[1,0,1]
	v_add_f32_e32 v27, 1.0, v27
	v_rcp_f32_e32 v27, v27
	s_nop 0
	v_mul_f32_e32 v19, v19, v27
	v_mul_f32_e32 v26, v26, v19
	v_min_f32_e32 v19, 0x40e00000, v29
	v_mul_f32_e32 v28, 0xc01d265f, v19
	v_exp_f32_e32 v28, v28
	v_med3_f32 v27, v35, s93, v242
	v_add_f32_e32 v27, 1.0, v27
	v_pk_fma_f32 v[34:35], v[106:107], s[38:39], v[6:7] op_sel_hi:[1,0,1]
	v_add_f32_e32 v28, 1.0, v28
	v_rcp_f32_e32 v28, v28
	v_med3_f32 v34, v34, s93, v242
	v_add_f32_e32 v34, 1.0, v34
	v_mul_f32_e32 v19, v19, v28
	v_mul_f32_e32 v27, v27, v19
	v_min_f32_e32 v19, 0x40e00000, v20
	v_med3_f32 v20, v24, s93, v242
	v_mul_f32_e32 v24, 0xc01d265f, v19
	v_exp_f32_e32 v24, v24
	v_pk_fma_f32 v[28:29], v[114:115], s[38:39], v[14:15] op_sel_hi:[1,0,1]
	v_add_f32_e32 v20, 1.0, v20
	v_min_f32_e32 v28, 0x40e00000, v28
	v_add_f32_e32 v24, 1.0, v24
	v_rcp_f32_e32 v24, v24
	v_mul_f32_e32 v38, 0xc01d265f, v28
	v_exp_f32_e32 v38, v38
	v_mul_f32_e32 v19, v19, v24
	v_mul_f32_e32 v20, v20, v19
	v_min_f32_e32 v19, 0x40e00000, v21
	v_mul_f32_e32 v24, 0xc01d265f, v19
	v_add_f32_e32 v38, 1.0, v38
	v_exp_f32_e32 v24, v24
	v_rcp_f32_e32 v38, v38
	v_min_f32_e32 v29, 0x40e00000, v29
	v_med3_f32 v21, v25, s93, v242
	v_add_f32_e32 v24, 1.0, v24
	v_mul_f32_e32 v28, v28, v38
	v_rcp_f32_e32 v24, v24
	v_mul_f32_e32 v28, v34, v28
	v_med3_f32 v34, v35, s93, v242
	v_mul_f32_e32 v35, 0xc01d265f, v29
	v_exp_f32_e32 v35, v35
	v_mul_f32_e32 v19, v19, v24
	v_add_f32_e32 v21, 1.0, v21
	v_mul_f32_e32 v21, v21, v19
	v_mov_b32_e32 v19, v67
	v_cvt_pk_fp8_f32 v19, v26, v27
	v_add_f32_e32 v35, 1.0, v35
	v_rcp_f32_e32 v35, v35
	v_add_f32_e32 v34, 1.0, v34
	v_cvt_pk_fp8_f32 v19, v20, v21 op_sel:[0,0,1]
	v_pk_fma_f32 v[20:21], v[116:117], s[38:39], v[16:17] op_sel_hi:[1,0,1]
	v_mul_f32_e32 v29, v29, v35
	v_min_f32_e32 v20, 0x40e00000, v20
	v_mul_f32_e32 v29, v34, v29
	v_mul_f32_e32 v34, 0xc01d265f, v20
	v_exp_f32_e32 v34, v34
	v_pk_fma_f32 v[24:25], v[112:113], s[38:39], v[12:13] op_sel_hi:[1,0,1]
	v_pk_fma_f32 v[26:27], v[104:105], s[38:39], v[4:5] op_sel_hi:[1,0,1]
	v_add_f32_e32 v34, 1.0, v34
	v_rcp_f32_e32 v34, v34
	s_nop 0
	v_mul_f32_e32 v20, v20, v34
	v_mul_f32_e32 v32, v32, v20
	v_min_f32_e32 v20, 0x40e00000, v21
	v_med3_f32 v21, v33, s93, v242
	v_mul_f32_e32 v33, 0xc01d265f, v20
	v_exp_f32_e32 v33, v33
	v_add_f32_e32 v21, 1.0, v21
	v_pk_fma_f32 v[34:35], v[90:91], s[38:39], v[2:3] op_sel_hi:[1,0,1]
	v_pk_fma_f32 v[2:3], v[78:79], s[38:39], v[2:3] op_sel_hi:[1,0,1]
	v_add_f32_e32 v33, 1.0, v33
	v_rcp_f32_e32 v33, v33
	v_med3_f32 v2, v2, s93, v242
	v_add_f32_e32 v2, 1.0, v2
	v_med3_f32 v3, v3, s93, v242
	v_mul_f32_e32 v20, v20, v33
	v_mul_f32_e32 v21, v21, v20
	v_mov_b32_e32 v20, v67
	v_cvt_pk_fp8_f32 v20, v28, v29
	v_med3_f32 v28, v36, s93, v242
	v_add_f32_e32 v28, 1.0, v28
	v_add_f32_e32 v3, 1.0, v3
	v_cvt_pk_fp8_f32 v20, v32, v21 op_sel:[0,0,1]
	v_min_f32_e32 v21, 0x40e00000, v30
	v_mul_f32_e32 v29, 0xc01d265f, v21
	v_exp_f32_e32 v29, v29
	v_pk_fma_f32 v[32:33], v[94:95], s[38:39], v[6:7] op_sel_hi:[1,0,1]
	v_permlane32_swap_b32_e32 v18, v20
	v_add_f32_e32 v29, 1.0, v29
	v_rcp_f32_e32 v29, v29
	v_med3_f32 v32, v32, s93, v242
	v_add_f32_e32 v32, 1.0, v32
	v_pk_fma_f32 v[6:7], v[82:83], s[38:39], v[6:7] op_sel_hi:[1,0,1]
	v_mul_f32_e32 v21, v21, v29
	v_mul_f32_e32 v28, v28, v21
	v_min_f32_e32 v21, 0x40e00000, v31
	v_mul_f32_e32 v30, 0xc01d265f, v21
	v_exp_f32_e32 v30, v30
	v_med3_f32 v29, v37, s93, v242
	v_add_f32_e32 v29, 1.0, v29
	v_med3_f32 v6, v6, s93, v242
	v_add_f32_e32 v30, 1.0, v30
	v_rcp_f32_e32 v30, v30
	v_add_f32_e32 v6, 1.0, v6
	v_med3_f32 v7, v7, s93, v242
	v_add_f32_e32 v7, 1.0, v7
	v_mul_f32_e32 v21, v21, v30
	v_mul_f32_e32 v29, v29, v21
	v_min_f32_e32 v21, 0x40e00000, v24
	v_med3_f32 v24, v26, s93, v242
	v_mul_f32_e32 v26, 0xc01d265f, v21
	v_exp_f32_e32 v26, v26
	v_add_f32_e32 v24, 1.0, v24
	v_pk_fma_f32 v[30:31], v[96:97], s[38:39], v[8:9] op_sel_hi:[1,0,1]
	v_pk_fma_f32 v[8:9], v[84:85], s[38:39], v[8:9] op_sel_hi:[1,0,1]
	v_add_f32_e32 v26, 1.0, v26
	v_rcp_f32_e32 v26, v26
	v_med3_f32 v30, v30, s93, v242
	v_add_f32_e32 v30, 1.0, v30
	v_med3_f32 v8, v8, s93, v242
	v_mul_f32_e32 v21, v21, v26
	v_mul_f32_e32 v24, v24, v21
	v_min_f32_e32 v21, 0x40e00000, v25
	v_mul_f32_e32 v26, 0xc01d265f, v21
	v_exp_f32_e32 v26, v26
	v_med3_f32 v25, v27, s93, v242
	v_add_f32_e32 v25, 1.0, v25
	v_add_f32_e32 v8, 1.0, v8
	v_add_f32_e32 v26, 1.0, v26
	v_rcp_f32_e32 v26, v26
	v_med3_f32 v9, v9, s93, v242
	v_add_f32_e32 v9, 1.0, v9
	v_mul_f32_e32 v21, v21, v26
	v_pk_fma_f32 v[26:27], v[98:99], s[38:39], v[14:15] op_sel_hi:[1,0,1]
	v_mul_f32_e32 v25, v25, v21
	v_min_f32_e32 v26, 0x40e00000, v26
	v_mul_f32_e32 v36, 0xc01d265f, v26
	v_exp_f32_e32 v36, v36
	v_min_f32_e32 v27, 0x40e00000, v27
	v_mov_b32_e32 v21, v67
	v_cvt_pk_fp8_f32 v21, v28, v29
	v_add_f32_e32 v36, 1.0, v36
	v_rcp_f32_e32 v36, v36
	v_pk_fma_f32 v[28:29], v[86:87], s[38:39], v[10:11] op_sel_hi:[1,0,1]
	v_cvt_pk_fp8_f32 v21, v24, v25 op_sel:[0,0,1]
	v_add_u32_e32 v24, s83, v220
	v_mul_f32_e32 v26, v26, v36
	v_mul_f32_e32 v26, v32, v26
	v_med3_f32 v32, v33, s93, v242
	v_mul_f32_e32 v33, 0xc01d265f, v27
	v_exp_f32_e32 v33, v33
	v_ashrrev_i32_e32 v25, 31, v24
	v_lshlrev_b64 v[24:25], 11, v[24:25]
	v_lshl_add_u64 v[24:25], s[12:13], 0, v[24:25]
	v_add_f32_e32 v33, 1.0, v33
	v_rcp_f32_e32 v33, v33
	v_permlane32_swap_b32_e32 v19, v21
	v_lshl_add_u64 v[24:25], v[24:25], 0, v[22:23]
	global_store_dwordx4 v[24:25], v[18:21], off
	v_mul_f32_e32 v27, v27, v33
	v_add_f32_e32 v32, 1.0, v32
	v_pk_fma_f32 v[18:19], v[100:101], s[38:39], v[16:17] op_sel_hi:[1,0,1]
	v_mul_f32_e32 v27, v32, v27
	v_min_f32_e32 v18, 0x40e00000, v18
	v_mul_f32_e32 v32, 0xc01d265f, v18
	v_exp_f32_e32 v32, v32
	v_pk_fma_f32 v[20:21], v[88:89], s[38:39], v[12:13] op_sel_hi:[1,0,1]
	v_pk_fma_f32 v[24:25], v[92:93], s[38:39], v[4:5] op_sel_hi:[1,0,1]
	v_pk_fma_f32 v[14:15], v[74:75], s[38:39], v[14:15] op_sel_hi:[1,0,1]
	v_add_f32_e32 v32, 1.0, v32
	v_rcp_f32_e32 v32, v32
	v_min_f32_e32 v14, 0x40e00000, v14
	v_pk_fma_f32 v[10:11], v[70:71], s[38:39], v[10:11] op_sel_hi:[1,0,1]
	v_pk_fma_f32 v[16:17], v[76:77], s[38:39], v[16:17] op_sel_hi:[1,0,1]
	v_mul_f32_e32 v18, v18, v32
	v_mul_f32_e32 v30, v30, v18
	v_min_f32_e32 v18, 0x40e00000, v19
	v_med3_f32 v19, v31, s93, v242
	v_mul_f32_e32 v31, 0xc01d265f, v18
	v_exp_f32_e32 v31, v31
	v_add_f32_e32 v19, 1.0, v19
	v_pk_fma_f32 v[12:13], v[72:73], s[38:39], v[12:13] op_sel_hi:[1,0,1]
	v_pk_fma_f32 v[4:5], v[80:81], s[38:39], v[4:5] op_sel_hi:[1,0,1]
	v_add_f32_e32 v31, 1.0, v31
	v_rcp_f32_e32 v31, v31
	v_med3_f32 v4, v4, s93, v242
	v_add_f32_e32 v4, 1.0, v4
	v_med3_f32 v5, v5, s93, v242
	v_mul_f32_e32 v18, v18, v31
	v_mul_f32_e32 v19, v19, v18
	v_mov_b32_e32 v18, v67
	v_cvt_pk_fp8_f32 v18, v26, v27
	v_med3_f32 v26, v34, s93, v242
	v_add_f32_e32 v26, 1.0, v26
	v_add_f32_e32 v5, 1.0, v5
	v_cvt_pk_fp8_f32 v18, v30, v19 op_sel:[0,0,1]
	v_min_f32_e32 v19, 0x40e00000, v28
	v_mul_f32_e32 v27, 0xc01d265f, v19
	v_exp_f32_e32 v27, v27
	s_nop 0
	v_add_f32_e32 v27, 1.0, v27
	v_rcp_f32_e32 v27, v27
	s_nop 0
	v_mul_f32_e32 v19, v19, v27
	v_mul_f32_e32 v26, v26, v19
	v_min_f32_e32 v19, 0x40e00000, v29
	v_mul_f32_e32 v28, 0xc01d265f, v19
	v_exp_f32_e32 v28, v28
	v_med3_f32 v27, v35, s93, v242
	v_add_f32_e32 v27, 1.0, v27
	v_add_f32_e32 v28, 1.0, v28
	v_rcp_f32_e32 v28, v28
	s_nop 0
	v_mul_f32_e32 v19, v19, v28
	v_mul_f32_e32 v27, v27, v19
	v_min_f32_e32 v19, 0x40e00000, v20
	v_med3_f32 v20, v24, s93, v242
	v_mul_f32_e32 v24, 0xc01d265f, v19
	v_exp_f32_e32 v24, v24
	v_add_f32_e32 v20, 1.0, v20
	v_add_f32_e32 v24, 1.0, v24
	v_rcp_f32_e32 v24, v24
	s_nop 0
	v_mul_f32_e32 v19, v19, v24
	v_mul_f32_e32 v20, v20, v19
	v_min_f32_e32 v19, 0x40e00000, v21
	v_mul_f32_e32 v24, 0xc01d265f, v19
	v_exp_f32_e32 v24, v24
	v_med3_f32 v21, v25, s93, v242
	v_add_f32_e32 v21, 1.0, v21
	v_add_f32_e32 v24, 1.0, v24
	v_rcp_f32_e32 v24, v24
	s_nop 0
	v_mul_f32_e32 v19, v19, v24
	v_mul_f32_e32 v21, v21, v19
	v_mov_b32_e32 v19, v67
	v_cvt_pk_fp8_f32 v19, v26, v27
	v_cvt_pk_fp8_f32 v19, v20, v21 op_sel:[0,0,1]
	v_mul_f32_e32 v20, 0xc01d265f, v14
	v_exp_f32_e32 v20, v20
	v_mov_b32_e32 v21, v67
	v_add_f32_e32 v20, 1.0, v20
	v_rcp_f32_e32 v20, v20
	s_nop 0
	v_mul_f32_e32 v14, v14, v20
	v_mul_f32_e32 v6, v6, v14
	v_min_f32_e32 v14, 0x40e00000, v15
	v_mul_f32_e32 v15, 0xc01d265f, v14
	v_exp_f32_e32 v15, v15
	v_mov_b32_e32 v20, v67
	v_add_f32_e32 v15, 1.0, v15
	v_rcp_f32_e32 v15, v15
	s_nop 0
	v_mul_f32_e32 v14, v14, v15
	v_mul_f32_e32 v7, v7, v14
	v_cvt_pk_fp8_f32 v20, v6, v7
	v_min_f32_e32 v6, 0x40e00000, v10
	v_mul_f32_e32 v7, 0xc01d265f, v6
	v_exp_f32_e32 v7, v7
	v_min_f32_e32 v14, 0x40e00000, v16
	v_mul_f32_e32 v15, 0xc01d265f, v14
	v_add_f32_e32 v7, 1.0, v7
	v_rcp_f32_e32 v7, v7
	v_exp_f32_e32 v15, v15
	v_mul_f32_e32 v6, v6, v7
	v_mul_f32_e32 v2, v2, v6
	v_min_f32_e32 v6, 0x40e00000, v11
	v_mul_f32_e32 v7, 0xc01d265f, v6
	v_exp_f32_e32 v7, v7
	v_add_f32_e32 v15, 1.0, v15
	v_rcp_f32_e32 v15, v15
	v_add_f32_e32 v7, 1.0, v7
	v_rcp_f32_e32 v7, v7
	v_mul_f32_e32 v14, v14, v15
	v_mul_f32_e32 v8, v8, v14
	v_min_f32_e32 v14, 0x40e00000, v17
	v_mul_f32_e32 v6, v6, v7
	v_mul_f32_e32 v3, v3, v6
	v_min_f32_e32 v6, 0x40e00000, v12
	v_mul_f32_e32 v7, 0xc01d265f, v6
	v_exp_f32_e32 v7, v7
	v_mul_f32_e32 v15, 0xc01d265f, v14
	v_exp_f32_e32 v15, v15
	v_add_f32_e32 v7, 1.0, v7
	v_rcp_f32_e32 v7, v7
	v_cvt_pk_fp8_f32 v21, v2, v3
	v_add_f32_e32 v15, 1.0, v15
	v_rcp_f32_e32 v15, v15
	v_mul_f32_e32 v6, v6, v7
	v_mul_f32_e32 v4, v4, v6
	v_min_f32_e32 v6, 0x40e00000, v13
	v_mul_f32_e32 v7, 0xc01d265f, v6
	v_exp_f32_e32 v7, v7
	v_mul_f32_e32 v14, v14, v15
	v_mul_f32_e32 v9, v9, v14
	v_cvt_pk_fp8_f32 v20, v8, v9 op_sel:[0,0,1]
	v_add_f32_e32 v7, 1.0, v7
	v_rcp_f32_e32 v7, v7
	v_add_u32_e32 v2, s83, v221
	v_ashrrev_i32_e32 v3, 31, v2
	v_lshlrev_b64 v[2:3], 11, v[2:3]
	v_mul_f32_e32 v6, v6, v7
	v_mul_f32_e32 v5, v5, v6
	v_cvt_pk_fp8_f32 v21, v4, v5 op_sel:[0,0,1]
	v_lshl_add_u64 v[2:3], s[12:13], 0, v[2:3]
	v_permlane32_swap_b32_e32 v18, v20
	v_permlane32_swap_b32_e32 v19, v21
	v_lshl_add_u64 v[2:3], v[2:3], 0, v[22:23]
	global_store_dwordx4 v[2:3], v[18:21], off
	s_cmp_lg_u32 s92, s68
	s_cbranch_scc1 .LBB0_1140
